# topk int8 packing: rndne+cvt+shift/mask/or3 (13 VALU per dword) replaced by magic-number add + three v_perm_b32 (7 VALU), bit-identical results
# speedup vs baseline: 1.0045x; 1.0045x over previous
.LBB0_1844:
	v_readlane_b32 s0, v253, 60
	v_readlane_b32 s1, v253, 61
	s_andn2_b64 vcc, exec, s[0:1]
	s_cbranch_vccnz .LBB0_1876
	v_and_b32_e32 v33, -8, v32
	v_cmp_eq_u32_e64 s[44:45], 16, v33
	v_subrev_u32_e32 v46, 24, v32
	v_subrev_u32_e32 v47, 29, v32
	v_cndmask_b32_e64 v51, 0, 4, s[44:45]
	v_cmp_lt_u32_e64 s[44:45], 4, v46
	v_subrev_u32_e32 v48, 33, v32
	v_and_b32_e32 v49, -2, v32
	v_cndmask_b32_e64 v46, 8, v51, s[44:45]
	v_cmp_lt_u32_e64 s[44:45], 3, v47
	v_cmp_eq_u32_e32 vcc, 1, v32
	s_mov_b32 s0, s38
	v_cndmask_b32_e64 v46, 12, v46, s[44:45]
	v_cmp_lt_u32_e64 s[44:45], 2, v48
	v_writelane_b32 v255, s0, 45
	v_readlane_b32 s8, v251, 38
	v_cndmask_b32_e64 v46, 16, v46, s[44:45]
	v_cmp_ne_u32_e64 s[44:45], 36, v49
	v_writelane_b32 v255, s1, 46
	v_lshlrev_b32_e32 v44, 4, v32
	v_cndmask_b32_e64 v46, 20, v46, s[44:45]
	v_cmp_ne_u32_e64 s[44:45], 38, v49
	v_readlane_b32 s9, v251, 39
	v_lshlrev_b32_e32 v36, 5, v32
	v_cndmask_b32_e64 v46, 24, v46, s[44:45]
	v_cmp_ne_u32_e64 s[44:45], 40, v49
	v_lshlrev_b32_e32 v38, 3, v32
	v_add_u32_e32 v42, 0x400, v44
	v_cndmask_b32_e64 v46, 28, v46, s[44:45]
	v_cmp_ne_u32_e64 s[44:45], 42, v32
	v_readlane_b32 s8, v255, 4
	v_ashrrev_i32_e32 v37, 31, v36
	v_cndmask_b32_e64 v46, 32, v46, s[44:45]
	v_cmp_ne_u32_e64 s[44:45], 43, v32
	v_and_b32_e32 v139, 0x78, v38
	v_and_b32_e32 v100, 0xffffff80, v38
	v_cndmask_b32_e64 v46, 36, v46, s[44:45]
	v_cmp_ne_u32_e64 s[44:45], 44, v32
	v_ashrrev_i32_e32 v38, 3, v32
	v_ashrrev_i32_e32 v42, 7, v42
	v_cndmask_b32_e64 v46, 40, v46, s[44:45]
	v_cmp_ne_u32_e64 s[44:45], 45, v32
	v_readlane_b32 s9, v255, 5
	s_lshl_b32 s4, s38, 11
	v_cndmask_b32_e64 v46, 44, v46, s[44:45]
	v_cmp_ne_u32_e64 s[44:45], 46, v32
	v_ashrrev_i32_e32 v39, 31, v38
	v_ashrrev_i32_e32 v43, 31, v42
	v_cndmask_b32_e64 v46, 48, v46, s[44:45]
	v_cmp_ne_u32_e64 s[44:45], 47, v32
	v_lshl_add_u64 v[122:123], s[8:9], 0, v[36:37]
	v_readlane_b32 s8, v255, 10
	v_cndmask_b32_e64 v46, 52, v46, s[44:45]
	v_cmp_ne_u32_e64 s[44:45], 48, v32
	s_cmp_lg_u32 s38, 3
	v_lshlrev_b64 v[40:41], 21, v[38:39]
	v_cndmask_b32_e64 v46, 56, v46, s[44:45]
	v_cmp_ne_u32_e64 s[44:45], 49, v32
	v_lshlrev_b64 v[42:43], 21, v[42:43]
	v_readlane_b32 s9, v255, 11
	v_cndmask_b32_e64 v146, 60, v46, s[44:45]
	v_cndmask_b32_e64 v46, 0, 4, vcc
	v_cmp_ne_u32_e32 vcc, 2, v32
	s_cselect_b64 s[68:69], -1, 0
	s_add_i32 s94, s4, 0x800
	v_cndmask_b32_e32 v46, 8, v46, vcc
	v_cmp_ne_u32_e32 vcc, 3, v32
	v_lshl_add_u64 v[124:125], s[8:9], 0, v[42:43]
	v_lshl_add_u64 v[126:127], s[8:9], 0, v[40:41]
	v_cndmask_b32_e32 v46, 12, v46, vcc
	v_cmp_ne_u32_e32 vcc, 4, v32
	v_readlane_b32 s8, v255, 18
	s_mov_b64 s[62:63], s[52:53]
	v_cndmask_b32_e32 v46, 16, v46, vcc
	v_cmp_ne_u32_e32 vcc, 5, v32
	s_lshl_b64 s[52:53], s[94:95], 2
	v_readlane_b32 s20, v251, 50
	v_cndmask_b32_e32 v46, 20, v46, vcc
	v_cmp_ne_u32_e32 vcc, 6, v32
	v_readlane_b32 s9, v255, 19
	v_subrev_u32_e32 v50, 42, v32
	v_cndmask_b32_e32 v46, 24, v46, vcc
	v_cmp_ne_u32_e32 vcc, 7, v32
	v_ashrrev_i32_e32 v33, 31, v32
	v_ashrrev_i32_e32 v45, 31, v44
	v_cndmask_b32_e32 v46, 28, v46, vcc
	v_cmp_ne_u32_e32 vcc, 8, v32
	v_readlane_b32 s21, v251, 51
	s_add_u32 s52, s20, s52
	v_cndmask_b32_e32 v46, 32, v46, vcc
	v_cmp_ne_u32_e32 vcc, 9, v32
	v_lshl_add_u64 v[128:129], s[8:9], 0, v[42:43]
	v_lshl_add_u64 v[130:131], s[8:9], 0, v[40:41]
	v_cndmask_b32_e32 v46, 36, v46, vcc
	v_cmp_ne_u32_e32 vcc, 10, v32
	v_readlane_b32 s8, v255, 24
	v_lshlrev_b64 v[34:35], 2, v[32:33]
	v_cndmask_b32_e32 v46, 40, v46, vcc
	v_cmp_ne_u32_e32 vcc, 11, v32
	v_ashrrev_i32_e32 v33, 4, v32
	s_addc_u32 s53, s21, s53
	v_cndmask_b32_e32 v46, 44, v46, vcc
	v_cmp_ne_u32_e32 vcc, 12, v32
	v_lshlrev_b64 v[110:111], 2, v[44:45]
	v_readlane_b32 s9, v255, 25
	v_cndmask_b32_e32 v46, 48, v46, vcc
	v_cmp_ne_u32_e32 vcc, 13, v32
	v_cmp_gt_u32_e64 s[4:5], 50, v32
	v_cmp_eq_u32_e64 s[78:79], 0, v32
	v_cndmask_b32_e32 v46, 52, v46, vcc
	v_cmp_ne_u32_e32 vcc, 14, v32
	v_cmp_gt_i32_e64 s[76:77], 32, v32
	v_and_b32_e32 v140, 15, v32
	v_cndmask_b32_e32 v46, 56, v46, vcc
	v_cmp_ne_u32_e32 vcc, 15, v32
	v_sub_u32_e32 v141, 63, v32
	v_lshl_add_u32 v142, v32, 2, s84
	v_cndmask_b32_e32 v46, 60, v46, vcc
	v_cmp_ne_u32_e32 vcc, 16, v32
	v_cmp_gt_u32_e64 s[44:45], 16, v32
	v_cmp_eq_u32_e64 s[46:47], 1, v33
	v_cndmask_b32_e32 v46, 0, v46, vcc
	v_cmp_ne_u32_e32 vcc, 17, v32
	v_cmp_eq_u32_e64 s[48:49], 2, v33
	v_cmp_eq_u32_e64 s[50:51], 3, v33
	v_cndmask_b32_e32 v46, 4, v46, vcc
	v_cmp_ne_u32_e32 vcc, 18, v32
	v_add_u32_e32 v33, 64, v32
	v_lshl_add_u64 v[112:113], s[52:53], 0, v[110:111]
	v_cndmask_b32_e32 v46, 8, v46, vcc
	v_cmp_ne_u32_e32 vcc, 19, v32
	s_mov_b64 s[52:53], 0x1010
	v_lshl_add_u64 v[132:133], s[8:9], 0, v[34:35]
	v_cndmask_b32_e32 v46, 12, v46, vcc
	v_cmp_ne_u32_e32 vcc, 20, v32
	v_readlane_b32 s8, v255, 26
	v_readlane_b32 s18, v251, 48
	v_cndmask_b32_e32 v46, 16, v46, vcc
	v_cmp_ne_u32_e32 vcc, 21, v32
	v_readlane_b32 s19, v251, 49
	v_readlane_b32 s22, v251, 52
	v_cndmask_b32_e32 v46, 20, v46, vcc
	v_cmp_ne_u32_e32 vcc, 22, v32
	v_readlane_b32 s23, v251, 53
	v_lshl_add_u64 v[116:117], v[112:113], 0, s[52:53]
	v_cndmask_b32_e32 v46, 24, v46, vcc
	v_cmp_ne_u32_e32 vcc, 23, v32
	s_mov_b64 s[52:53], 0x1020
	v_readlane_b32 s9, v255, 27
	v_cndmask_b32_e32 v46, 28, v46, vcc
	v_cmp_ne_u32_e32 vcc, 24, v32
	v_lshlrev_b32_e32 v200, 1, v139
	v_add_u32_e32 v104, 0x200, v100
	v_cndmask_b32_e32 v46, 0, v46, vcc
	v_cmp_ne_u32_e32 vcc, 25, v32
	v_add_u32_e32 v106, 0x400, v100
	v_add_u32_e32 v108, 0x600, v100
	v_cndmask_b32_e32 v46, 4, v46, vcc
	v_cmp_ne_u32_e32 vcc, 26, v32
	v_readlane_b32 s12, v251, 42
	v_readlane_b32 s13, v251, 43
	v_cndmask_b32_e32 v46, 8, v46, vcc
	v_cmp_ne_u32_e32 vcc, 27, v32
	v_readlane_b32 s14, v251, 44
	v_readlane_b32 s15, v251, 45
	v_cndmask_b32_e32 v46, 12, v46, vcc
	v_cmp_ne_u32_e32 vcc, 28, v32
	s_mov_b64 s[22:23], s[76:77]
	s_mov_b64 s[18:19], s[68:69]
	v_cndmask_b32_e32 v46, 16, v46, vcc
	v_cmp_ne_u32_e32 vcc, 29, v32
	v_lshl_add_u64 v[118:119], v[112:113], 0, s[52:53]
	s_mov_b64 s[52:53], 0x1030
	v_cndmask_b32_e32 v46, 0, v46, vcc
	v_cmp_ne_u32_e32 vcc, 30, v32
	v_readlane_b32 s68, v255, 16
	v_readlane_b32 s76, v254, 62
	v_cndmask_b32_e32 v46, 4, v46, vcc
	v_cmp_ne_u32_e32 vcc, 31, v32
	s_waitcnt vmcnt(0)
	v_lshl_add_u64 v[96:97], s[66:67], 0, v[34:35]
	v_lshl_add_u64 v[98:99], v[36:37], 1, s[70:71]
	v_cndmask_b32_e32 v46, 8, v46, vcc
	v_cmp_ne_u32_e32 vcc, 32, v32
	v_lshl_add_u64 v[102:103], s[96:97], 0, v[200:201]
	v_and_b32_e32 v200, 0x70, v44
	v_cndmask_b32_e32 v46, 12, v46, vcc
	v_cmp_ne_u32_e32 vcc, 33, v32
	v_or_b32_e32 v143, 1, v139
	v_or_b32_e32 v144, 2, v139
	v_cndmask_b32_e32 v46, 0, v46, vcc
	v_cmp_ne_u32_e32 vcc, 34, v32
	v_or_b32_e32 v145, 3, v139
	v_ashrrev_i32_e32 v101, 31, v100
	v_cndmask_b32_e32 v46, 4, v46, vcc
	v_cmp_ne_u32_e32 vcc, 35, v32
	v_ashrrev_i32_e32 v105, 31, v104
	v_ashrrev_i32_e32 v107, 31, v106
	v_cndmask_b32_e32 v46, 8, v46, vcc
	v_cmp_ne_u32_e32 vcc, 36, v32
	v_ashrrev_i32_e32 v109, 31, v108
	v_cmp_eq_u32_e64 s[0:1], 0, v140
	v_cndmask_b32_e32 v46, 0, v46, vcc
	v_cmp_ne_u32_e32 vcc, 37, v32
	v_cmp_eq_u32_e64 s[54:55], 1, v140
	v_cmp_eq_u32_e64 s[64:65], 2, v140
	v_cndmask_b32_e32 v46, 4, v46, vcc
	v_cmp_ne_u32_e32 vcc, 38, v32
	v_cmp_eq_u32_e64 s[2:3], 3, v140
	v_cmp_eq_u32_e64 s[6:7], 4, v140
	v_cndmask_b32_e32 v46, 0, v46, vcc
	v_cmp_ne_u32_e32 vcc, 39, v32
	v_cmp_eq_u32_e64 s[96:97], 5, v140
	v_cmp_eq_u32_e64 s[66:67], 6, v140
	v_cndmask_b32_e32 v46, 4, v46, vcc
	v_cmp_ne_u32_e32 vcc, 40, v32
	v_cmp_eq_u32_e64 s[24:25], 7, v140
	v_cmp_eq_u32_e64 s[26:27], 8, v140
	v_cndmask_b32_e32 v46, 0, v46, vcc
	v_cmp_ne_u32_e32 vcc, 41, v32
	v_and_b32_e32 v32, 7, v32
	v_lshlrev_b32_e32 v32, 6, v32
	v_cndmask_b32_e32 v46, 4, v46, vcc
	v_cmp_lt_u32_e32 vcc, 7, v50
	v_cmp_eq_u32_e64 s[28:29], 9, v140
	v_cmp_eq_u32_e64 s[30:31], 10, v140
	v_cndmask_b32_e32 v46, 0, v46, vcc
	v_add_u32_e32 v147, 64, v46
	v_add_u32_e32 v149, 0xc0, v46
	v_ashrrev_i32_e32 v46, 3, v33
	v_mov_b32_e32 v33, v201
	v_ashrrev_i32_e32 v47, 31, v46
	v_lshl_add_u64 v[32:33], s[8:9], 0, v[32:33]
	v_cmp_eq_u32_e64 s[34:35], 11, v140
	v_cmp_eq_u32_e64 s[36:37], 12, v140
	v_cmp_eq_u32_e64 s[38:39], 13, v140
	v_cmp_eq_u32_e64 s[40:41], 14, v140
	v_cmp_eq_u32_e64 s[42:43], 15, v140
	v_add_u32_e32 v148, 0x80, v146
	v_or_b32_e32 v150, 16, v140
	v_or_b32_e32 v151, 32, v140
	v_or_b32_e32 v152, 48, v140
	s_mov_b64 s[20:21], s[78:79]
	v_lshl_add_u64 v[114:115], v[112:113], 0, s[60:61]
	v_lshl_add_u64 v[120:121], v[112:113], 0, s[52:53]
	v_lshl_add_u64 v[134:135], v[38:39], 2, v[32:33]
	v_lshl_add_u64 v[136:137], v[46:47], 2, v[32:33]
	v_readlane_b32 s69, v255, 17
	s_mov_b64 s[14:15], s[62:63]
	s_mov_b64 s[12:13], s[74:75]
	v_readlane_b32 s77, v254, 63
	s_mov_b32 s8, s80
	v_readlane_b32 s10, v251, 40
	v_readlane_b32 s11, v251, 41
	v_readlane_b32 s16, v251, 46
	v_readlane_b32 s17, v251, 47
	v_mov_b32_e32 v226, 0x30c0400
	v_mov_b32_e32 v228, 0x3040100
	s_branch .LBB0_1848

.LBB0_1850:
	s_or_b64 exec, exec, s[52:53]
	v_lshlrev_b32_e32 v154, 16, v28
	v_and_b32_e32 v155, 0xffff0000, v28
	v_lshlrev_b32_e32 v28, 16, v29
	v_and_b32_e32 v29, 0xffff0000, v29
	v_pk_mul_f32 v[154:155], v[138:139], v[154:155] op_sel_hi:[0,1]
	v_pk_mul_f32 v[28:29], v[138:139], v[28:29] op_sel_hi:[0,1]
	v_med3_f32 v153, v154, s88, v236
	v_med3_f32 v154, v155, s88, v236
	v_med3_f32 v28, v28, s88, v236
	v_med3_f32 v29, v29, s88, v236
	v_add_f32_e32 v154, 0x4b400000, v154
	v_add_f32_e32 v153, 0x4b400000, v153
	v_add_f32_e32 v28, 0x4b400000, v28
	v_add_f32_e32 v29, 0x4b400000, v29
	s_mov_b32 s9, 0x40c0c00
	v_perm_b32 v29, v29, v153, s9
	v_perm_b32 v230, v154, v29, v226
	v_perm_b32 v28, v28, v230, v228
	v_lshlrev_b32_e32 v154, 16, v30
	v_and_b32_e32 v155, 0xffff0000, v30
	v_lshlrev_b32_e32 v30, 16, v31
	v_and_b32_e32 v31, 0xffff0000, v31
	v_pk_mul_f32 v[154:155], v[138:139], v[154:155] op_sel_hi:[0,1]
	v_pk_mul_f32 v[30:31], v[138:139], v[30:31] op_sel_hi:[0,1]
	v_med3_f32 v153, v155, s88, v236
	v_med3_f32 v29, v154, s88, v236
	v_med3_f32 v30, v30, s88, v236
	v_med3_f32 v31, v31, s88, v236
	v_add_f32_e32 v153, 0x4b400000, v153
	v_add_f32_e32 v29, 0x4b400000, v29
	v_add_f32_e32 v30, 0x4b400000, v30
	v_add_f32_e32 v31, 0x4b400000, v31
	v_perm_b32 v29, v31, v29, s9
	v_perm_b32 v230, v153, v29, v226
	v_perm_b32 v29, v30, v230, v228
	v_lshlrev_b32_e32 v30, 16, v24
	v_and_b32_e32 v31, 0xffff0000, v24
	v_lshlrev_b32_e32 v24, 16, v25
	v_and_b32_e32 v25, 0xffff0000, v25
	v_pk_mul_f32 v[30:31], v[138:139], v[30:31] op_sel_hi:[0,1]
	v_pk_mul_f32 v[24:25], v[138:139], v[24:25] op_sel_hi:[0,1]
	v_med3_f32 v31, v31, s88, v236
	v_med3_f32 v30, v30, s88, v236
	v_med3_f32 v24, v24, s88, v236
	v_med3_f32 v25, v25, s88, v236
	v_add_f32_e32 v31, 0x4b400000, v31
	v_add_f32_e32 v30, 0x4b400000, v30
	v_add_f32_e32 v24, 0x4b400000, v24
	v_add_f32_e32 v25, 0x4b400000, v25
	v_perm_b32 v25, v25, v30, s9
	v_perm_b32 v230, v31, v25, v226
	v_perm_b32 v30, v24, v230, v228
	v_lshlrev_b32_e32 v24, 16, v26
	v_and_b32_e32 v25, 0xffff0000, v26
	v_lshlrev_b32_e32 v26, 16, v27
	v_and_b32_e32 v27, 0xffff0000, v27
	v_pk_mul_f32 v[24:25], v[138:139], v[24:25] op_sel_hi:[0,1]
	v_pk_mul_f32 v[26:27], v[138:139], v[26:27] op_sel_hi:[0,1]
	v_med3_f32 v25, v25, s88, v236
	v_med3_f32 v24, v24, s88, v236
	v_med3_f32 v26, v26, s88, v236
	v_med3_f32 v27, v27, s88, v236
	v_add_f32_e32 v25, 0x4b400000, v25
	v_add_f32_e32 v24, 0x4b400000, v24
	v_add_f32_e32 v26, 0x4b400000, v26
	v_add_f32_e32 v27, 0x4b400000, v27
	v_perm_b32 v24, v27, v24, s9
	v_perm_b32 v230, v25, v24, v226
	v_perm_b32 v31, v26, v230, v228
	v_lshlrev_b32_e32 v24, 16, v20
	v_and_b32_e32 v25, 0xffff0000, v20
	v_lshlrev_b32_e32 v20, 16, v21
	v_and_b32_e32 v21, 0xffff0000, v21
	v_pk_mul_f32 v[24:25], v[138:139], v[24:25] op_sel_hi:[0,1]
	v_pk_mul_f32 v[20:21], v[138:139], v[20:21] op_sel_hi:[0,1]
	v_med3_f32 v25, v25, s88, v236
	v_med3_f32 v24, v24, s88, v236
	v_med3_f32 v20, v20, s88, v236
	v_med3_f32 v21, v21, s88, v236
	v_add_f32_e32 v25, 0x4b400000, v25
	v_add_f32_e32 v24, 0x4b400000, v24
	v_add_f32_e32 v20, 0x4b400000, v20
	v_add_f32_e32 v21, 0x4b400000, v21
	v_perm_b32 v21, v21, v24, s9
	v_perm_b32 v230, v25, v21, v226
	v_perm_b32 v20, v20, v230, v228
	v_lshlrev_b32_e32 v24, 16, v22
	v_and_b32_e32 v25, 0xffff0000, v22
	v_lshlrev_b32_e32 v22, 16, v23
	v_and_b32_e32 v23, 0xffff0000, v23
	v_pk_mul_f32 v[24:25], v[138:139], v[24:25] op_sel_hi:[0,1]
	v_pk_mul_f32 v[22:23], v[138:139], v[22:23] op_sel_hi:[0,1]
	v_med3_f32 v21, v24, s88, v236
	v_med3_f32 v24, v25, s88, v236
	v_med3_f32 v22, v22, s88, v236
	v_med3_f32 v23, v23, s88, v236
	v_add_f32_e32 v24, 0x4b400000, v24
	v_add_f32_e32 v21, 0x4b400000, v21
	v_add_f32_e32 v22, 0x4b400000, v22
	v_add_f32_e32 v23, 0x4b400000, v23
	v_perm_b32 v21, v23, v21, s9
	v_perm_b32 v230, v24, v21, v226
	v_perm_b32 v21, v22, v230, v228
	v_lshlrev_b32_e32 v22, 16, v16
	v_and_b32_e32 v23, 0xffff0000, v16
	v_lshlrev_b32_e32 v16, 16, v17
	v_and_b32_e32 v17, 0xffff0000, v17
	v_pk_mul_f32 v[22:23], v[138:139], v[22:23] op_sel_hi:[0,1]
	v_pk_mul_f32 v[16:17], v[138:139], v[16:17] op_sel_hi:[0,1]
	v_med3_f32 v23, v23, s88, v236
	v_med3_f32 v22, v22, s88, v236
	v_med3_f32 v16, v16, s88, v236
	v_med3_f32 v17, v17, s88, v236
	v_add_f32_e32 v23, 0x4b400000, v23
	v_add_f32_e32 v22, 0x4b400000, v22
	v_add_f32_e32 v16, 0x4b400000, v16
	v_add_f32_e32 v17, 0x4b400000, v17
	v_perm_b32 v17, v17, v22, s9
	v_perm_b32 v230, v23, v17, v226
	v_perm_b32 v22, v16, v230, v228
	v_lshlrev_b32_e32 v16, 16, v18
	v_and_b32_e32 v17, 0xffff0000, v18
	v_lshlrev_b32_e32 v18, 16, v19
	v_and_b32_e32 v19, 0xffff0000, v19
	v_pk_mul_f32 v[16:17], v[138:139], v[16:17] op_sel_hi:[0,1]
	v_pk_mul_f32 v[18:19], v[138:139], v[18:19] op_sel_hi:[0,1]
	v_med3_f32 v17, v17, s88, v236
	v_med3_f32 v16, v16, s88, v236
	v_med3_f32 v18, v18, s88, v236
	v_med3_f32 v19, v19, s88, v236
	v_add_f32_e32 v17, 0x4b400000, v17
	v_add_f32_e32 v16, 0x4b400000, v16
	s_nop 0
	v_add_f32_e32 v18, 0x4b400000, v18
	v_add_f32_e32 v19, 0x4b400000, v19
	s_nop 0
	s_nop 0
	s_nop 0
	v_readlane_b32 s10, v255, 20
	s_nop 0
	s_add_i32 s94, s80, s10
	s_nop 0
	s_nop 0
	v_perm_b32 v16, v19, v16, s9
	s_cmpk_gt_i32 s94, 0x3fff
	v_perm_b32 v230, v17, v16, v226
	v_perm_b32 v23, v18, v230, v228
	v_lshl_add_u64 v[16:17], s[92:93], 0, v[122:123]
	s_mov_b32 s52, 0x33200000
	s_cselect_b64 s[78:79], -1, 0
	s_cmpk_lt_i32 s94, 0x4000
	v_add_co_u32_e32 v16, vcc, s52, v16
	s_cselect_b32 s52, s94, s80
	s_nop 0
	v_addc_co_u32_e32 v17, vcc, 0, v17, vcc
	s_ashr_i32 s53, s52, 31
	v_mov_b32_e32 v138, 0
	global_store_dwordx4 v[16:17], v[28:31], off
	global_store_dwordx4 v[16:17], v[20:23], off offset:16
	v_readlane_b32 s11, v255, 21
	s_and_saveexec_b64 s[80:81], s[22:23]
	s_cbranch_execz .LBB0_1852
	s_lshl_b64 vcc, s[52:53], 7
	v_lshl_add_u64 v[16:17], v[96:97], 0, vcc
	global_load_dword v138, v[16:17], off

.LBB0_1871:
	s_waitcnt vmcnt(16)
	v_max_f32_e64 v153, |v47|, |v47|
	v_max_f32_e64 v154, |v46|, |v46|
	v_max_f32_e32 v153, v154, v153
	v_max_f32_e64 v154, |v43|, |v43|
	v_max_f32_e64 v155, |v42|, |v42|
	v_max_f32_e32 v154, v155, v154
	v_max3_f32 v153, |v44|, |v45|, v153
	v_max3_f32 v154, |v40|, |v41|, v154
	v_max3_f32 v153, v153, 0, v154
	v_max_f32_e64 v154, |v39|, |v39|
	v_max_f32_e64 v155, |v38|, |v38|
	v_max_f32_e32 v154, v155, v154
	v_max_f32_e64 v155, |v35|, |v35|
	v_max_f32_e64 v156, |v34|, |v34|
	v_max_f32_e32 v155, v156, v155
	v_max3_f32 v154, |v36|, |v37|, v154
	v_max3_f32 v155, |v32|, |v33|, v155
	v_max3_f32 v153, v153, v154, v155
	s_waitcnt vmcnt(15)
	v_max_f32_e64 v154, |v51|, |v51|
	v_max_f32_e64 v155, |v50|, |v50|
	v_max_f32_e32 v154, v155, v154
	s_waitcnt vmcnt(12)
	v_max_f32_e64 v155, |v63|, |v63|
	v_max_f32_e64 v156, |v62|, |v62|
	v_max_f32_e32 v155, v156, v155
	v_max3_f32 v154, |v48|, |v49|, v154
	v_max3_f32 v155, |v60|, |v61|, v155
	v_max3_f32 v153, v153, v154, v155
	v_max_f32_e64 v154, |v59|, |v59|
	v_max_f32_e64 v155, |v58|, |v58|
	v_max_f32_e32 v154, v155, v154
	v_max_f32_e64 v155, |v55|, |v55|
	v_max_f32_e64 v156, |v54|, |v54|
	v_max_f32_e32 v155, v156, v155
	v_max3_f32 v154, |v56|, |v57|, v154
	v_max3_f32 v155, |v52|, |v53|, v155
	v_max3_f32 v153, v153, v154, v155
	v_mov_b32_e32 v154, v201
	s_mov_b32 s9, 0x42fe0000
	s_nop 0
	v_mov_b32_dpp v154, v153 row_ror:1 row_mask:0xf bank_mask:0xf
	v_max_f32_e32 v154, v154, v154
	v_max_f32_e32 v153, v153, v154
	v_mov_b32_e32 v154, v201
	s_nop 1
	v_mov_b32_dpp v154, v153 row_ror:2 row_mask:0xf bank_mask:0xf
	v_max_f32_e32 v154, v154, v154
	v_max_f32_e32 v153, v153, v154
	v_mov_b32_e32 v154, v201
	s_nop 1
	v_mov_b32_dpp v154, v153 row_ror:4 row_mask:0xf bank_mask:0xf
	v_max_f32_e32 v154, v154, v154
	v_max_f32_e32 v153, v153, v154
	v_mov_b32_e32 v154, v201
	s_nop 1
	v_mov_b32_dpp v154, v153 row_ror:8 row_mask:0xf bank_mask:0xf
	v_max_f32_e32 v154, v154, v154
	v_max_f32_e32 v153, v153, v154
	v_mov_b32_e32 v154, v153
	s_nop 1
	v_permlane16_swap_b32_e32 v153, v154
	v_max_f32_e32 v154, v154, v154
	v_max_f32_e32 v153, v153, v153
	v_max_f32_e32 v153, v153, v154
	v_mov_b32_e32 v154, v153
	s_nop 1
	v_permlane32_swap_b32_e32 v153, v154
	v_max_f32_e32 v154, v154, v154
	v_max_f32_e32 v153, v153, v153
	v_max_f32_e32 v153, v153, v154
	v_div_scale_f32 v154, s[52:53], v153, v153, s9
	v_rcp_f32_e32 v155, v154
	s_add_u32 s52, s92, s74
	s_addc_u32 s53, s93, s75
	v_fma_f32 v156, -v154, v155, 1.0
	v_fmac_f32_e32 v155, v156, v155
	v_div_scale_f32 v156, vcc, s9, v153, s9
	v_mul_f32_e32 v157, v156, v155
	v_fma_f32 v158, -v154, v157, v156
	v_fmac_f32_e32 v157, v158, v155
	v_fma_f32 v154, -v154, v157, v156
	v_div_fmas_f32 v154, v154, v155, v157
	v_div_fixup_f32 v154, v154, v153, s9
	v_cmp_lt_f32_e32 vcc, 0, v153
	s_mov_b32 s9, 0x40c0c00
	s_nop 0
	v_cndmask_b32_e32 v158, 0, v154, vcc
	v_pk_mul_f32 v[156:157], v[44:45], v[158:159] op_sel_hi:[1,0]
	v_pk_mul_f32 v[154:155], v[46:47], v[158:159] op_sel_hi:[1,0]
	v_add_f32_e32 v157, 0x4b400000, v157
	v_add_f32_e32 v156, 0x4b400000, v156
	s_nop 0
	v_add_f32_e32 v154, 0x4b400000, v154
	v_add_f32_e32 v155, 0x4b400000, v155
	v_perm_b32 v155, v155, v156, s9
	v_pk_mul_f32 v[160:161], v[40:41], v[158:159] op_sel_hi:[1,0]
	v_perm_b32 v230, v157, v155, v226
	v_perm_b32 v154, v154, v230, v228
	v_pk_mul_f32 v[156:157], v[42:43], v[158:159] op_sel_hi:[1,0]
	v_add_f32_e32 v159, 0x4b400000, v161
	v_add_f32_e32 v155, 0x4b400000, v160
	v_add_f32_e32 v156, 0x4b400000, v156
	v_add_f32_e32 v157, 0x4b400000, v157
	v_perm_b32 v155, v157, v155, s9
	v_pk_mul_f32 v[160:161], v[36:37], v[158:159] op_sel_hi:[1,0]
	v_perm_b32 v230, v159, v155, v226
	v_perm_b32 v155, v156, v230, v228
	v_pk_mul_f32 v[156:157], v[38:39], v[158:159] op_sel_hi:[1,0]
	v_add_f32_e32 v159, 0x4b400000, v160
	v_add_f32_e32 v160, 0x4b400000, v161
	v_add_f32_e32 v156, 0x4b400000, v156
	v_add_f32_e32 v157, 0x4b400000, v157
	v_perm_b32 v157, v157, v159, s9
	v_pk_mul_f32 v[162:163], v[32:33], v[158:159] op_sel_hi:[1,0]
	v_perm_b32 v230, v160, v157, v226
	v_perm_b32 v156, v156, v230, v228
	v_pk_mul_f32 v[160:161], v[34:35], v[158:159] op_sel_hi:[1,0]
	v_add_f32_e32 v159, 0x4b400000, v163
	v_add_f32_e32 v157, 0x4b400000, v162
	v_add_f32_e32 v160, 0x4b400000, v160
	v_add_f32_e32 v161, 0x4b400000, v161
	s_nop 0
	v_perm_b32 v157, v161, v157, s9
	v_perm_b32 v230, v159, v157, v226
	v_perm_b32 v157, v160, v230, v228
	v_lshl_add_u64 v[160:161], v[130:131], 0, v[200:201]
	global_store_dwordx4 v[160:161], v[154:157], off
	v_pk_mul_f32 v[160:161], v[60:61], v[158:159] op_sel_hi:[1,0]
	s_nop 0
	v_pk_mul_f32 v[156:157], v[48:49], v[158:159] op_sel_hi:[1,0]
	v_pk_mul_f32 v[154:155], v[50:51], v[158:159] op_sel_hi:[1,0]
	v_add_f32_e32 v157, 0x4b400000, v157
	v_add_f32_e32 v156, 0x4b400000, v156
	s_nop 0
	v_add_f32_e32 v154, 0x4b400000, v154
	v_add_f32_e32 v155, 0x4b400000, v155
	v_perm_b32 v155, v155, v156, s9
	v_perm_b32 v230, v157, v155, v226
	v_perm_b32 v154, v154, v230, v228
	v_pk_mul_f32 v[156:157], v[62:63], v[158:159] op_sel_hi:[1,0]
	v_add_f32_e32 v159, 0x4b400000, v161
	v_add_f32_e32 v155, 0x4b400000, v160
	v_add_f32_e32 v156, 0x4b400000, v156
	v_add_f32_e32 v157, 0x4b400000, v157
	v_perm_b32 v155, v157, v155, s9
	v_pk_mul_f32 v[160:161], v[56:57], v[158:159] op_sel_hi:[1,0]
	v_perm_b32 v230, v159, v155, v226
	v_perm_b32 v155, v156, v230, v228
	v_pk_mul_f32 v[156:157], v[58:59], v[158:159] op_sel_hi:[1,0]
	v_add_f32_e32 v159, 0x4b400000, v160
	v_add_f32_e32 v160, 0x4b400000, v161
	v_add_f32_e32 v156, 0x4b400000, v156
	v_add_f32_e32 v157, 0x4b400000, v157
	s_nop 0
	s_nop 0
	v_perm_b32 v157, v157, v159, s9
	v_perm_b32 v230, v160, v157, v226
	v_perm_b32 v156, v156, v230, v228
	v_pk_mul_f32 v[160:161], v[54:55], v[158:159] op_sel_hi:[1,0]
	v_pk_mul_f32 v[158:159], v[52:53], v[158:159] op_sel_hi:[1,0]
	s_nop 0
	v_add_f32_e32 v157, 0x4b400000, v158
	v_add_f32_e32 v158, 0x4b400000, v159
	s_nop 0
	v_add_f32_e32 v159, 0x4b400000, v160
	v_add_f32_e32 v160, 0x4b400000, v161
	s_nop 0
	s_nop 0
	s_nop 0
	v_perm_b32 v157, v160, v157, s9
	v_perm_b32 v230, v158, v157, v226
	v_perm_b32 v157, v159, v230, v228
	v_lshl_add_u64 v[158:159], v[128:129], 0, v[200:201]
	global_store_dwordx4 v[158:159], v[154:157], off
	s_and_saveexec_b64 s[80:81], s[20:21]
	s_cbranch_execz .LBB0_1873
	v_mul_f32_e32 v153, 0x3c010204, v153
	v_mov_b32_e32 v154, 0x850000
	global_store_dword v154, v153, s[52:53]
.LBB0_1873:
	s_or_b64 exec, exec, s[80:81]
	s_waitcnt vmcnt(13)
	v_max_f32_e64 v153, |v67|, |v67|
	v_max_f32_e64 v154, |v66|, |v66|
	v_max_f32_e32 v153, v154, v153
	s_waitcnt vmcnt(10)
	v_max_f32_e64 v154, |v79|, |v79|
	v_max_f32_e64 v155, |v78|, |v78|
	v_max_f32_e32 v154, v155, v154
	v_max3_f32 v153, |v64|, |v65|, v153
	v_max3_f32 v154, |v76|, |v77|, v154
	v_max3_f32 v153, v153, 0, v154
	v_max_f32_e64 v154, |v75|, |v75|
	v_max_f32_e64 v155, |v74|, |v74|
	v_max_f32_e32 v154, v155, v154
	v_max_f32_e64 v155, |v71|, |v71|
	v_max_f32_e64 v156, |v70|, |v70|
	v_max_f32_e32 v155, v156, v155
	v_max3_f32 v154, |v72|, |v73|, v154
	v_max3_f32 v155, |v68|, |v69|, v155
	v_max3_f32 v153, v153, v154, v155
	s_waitcnt vmcnt(9)
	v_max_f32_e64 v154, |v83|, |v83|
	v_max_f32_e64 v155, |v82|, |v82|
	v_max_f32_e32 v154, v155, v154
	s_waitcnt vmcnt(6)
	v_max_f32_e64 v155, |v95|, |v95|
	v_max_f32_e64 v156, |v94|, |v94|
	v_max_f32_e32 v155, v156, v155
	v_max3_f32 v154, |v80|, |v81|, v154
	v_max3_f32 v155, |v92|, |v93|, v155
	v_max3_f32 v153, v153, v154, v155
	v_max_f32_e64 v154, |v91|, |v91|
	v_max_f32_e64 v155, |v90|, |v90|
	v_max_f32_e32 v154, v155, v154
	v_max_f32_e64 v155, |v87|, |v87|
	v_max_f32_e64 v156, |v86|, |v86|
	v_max_f32_e32 v155, v156, v155
	v_max3_f32 v154, |v88|, |v89|, v154
	v_max3_f32 v155, |v84|, |v85|, v155
	v_max3_f32 v153, v153, v154, v155
	v_mov_b32_e32 v154, v201
	s_mov_b32 s9, 0x42fe0000
	s_nop 0
	v_mov_b32_dpp v154, v153 row_ror:1 row_mask:0xf bank_mask:0xf
	v_max_f32_e32 v154, v154, v154
	v_max_f32_e32 v153, v153, v154
	v_mov_b32_e32 v154, v201
	s_nop 1
	v_mov_b32_dpp v154, v153 row_ror:2 row_mask:0xf bank_mask:0xf
	v_max_f32_e32 v154, v154, v154
	v_max_f32_e32 v153, v153, v154
	v_mov_b32_e32 v154, v201
	s_nop 1
	v_mov_b32_dpp v154, v153 row_ror:4 row_mask:0xf bank_mask:0xf
	v_max_f32_e32 v154, v154, v154
	v_max_f32_e32 v153, v153, v154
	v_mov_b32_e32 v154, v201
	s_nop 1
	v_mov_b32_dpp v154, v153 row_ror:8 row_mask:0xf bank_mask:0xf
	v_max_f32_e32 v154, v154, v154
	v_max_f32_e32 v153, v153, v154
	v_mov_b32_e32 v154, v153
	s_nop 1
	v_permlane16_swap_b32_e32 v153, v154
	v_max_f32_e32 v154, v154, v154
	v_max_f32_e32 v153, v153, v153
	v_max_f32_e32 v153, v153, v154
	v_mov_b32_e32 v154, v153
	s_nop 1
	v_permlane32_swap_b32_e32 v153, v154
	v_max_f32_e32 v154, v154, v154
	v_max_f32_e32 v153, v153, v153
	v_max_f32_e32 v153, v153, v154
	v_div_scale_f32 v154, s[80:81], v153, v153, s9
	v_rcp_f32_e32 v155, v154
	s_nop 0
	v_fma_f32 v156, -v154, v155, 1.0
	v_fmac_f32_e32 v155, v156, v155
	v_div_scale_f32 v156, vcc, s9, v153, s9
	v_mul_f32_e32 v157, v156, v155
	v_fma_f32 v158, -v154, v157, v156
	v_fmac_f32_e32 v157, v158, v155
	v_fma_f32 v154, -v154, v157, v156
	v_div_fmas_f32 v154, v154, v155, v157
	v_div_fixup_f32 v154, v154, v153, s9
	v_cmp_lt_f32_e32 vcc, 0, v153
	s_mov_b32 s9, 0x40c0c00
	s_nop 0
	v_cndmask_b32_e32 v158, 0, v154, vcc
	v_pk_mul_f32 v[156:157], v[64:65], v[158:159] op_sel_hi:[1,0]
	v_pk_mul_f32 v[154:155], v[66:67], v[158:159] op_sel_hi:[1,0]
	v_add_f32_e32 v157, 0x4b400000, v157
	v_add_f32_e32 v156, 0x4b400000, v156
	s_nop 0
	v_add_f32_e32 v154, 0x4b400000, v154
	v_add_f32_e32 v155, 0x4b400000, v155
	v_perm_b32 v155, v155, v156, s9
	v_pk_mul_f32 v[160:161], v[76:77], v[158:159] op_sel_hi:[1,0]
	v_perm_b32 v230, v157, v155, v226
	v_perm_b32 v154, v154, v230, v228
	v_pk_mul_f32 v[156:157], v[78:79], v[158:159] op_sel_hi:[1,0]
	v_add_f32_e32 v159, 0x4b400000, v161
	v_add_f32_e32 v155, 0x4b400000, v160
	v_add_f32_e32 v156, 0x4b400000, v156
	v_add_f32_e32 v157, 0x4b400000, v157
	v_perm_b32 v155, v157, v155, s9
	v_pk_mul_f32 v[160:161], v[72:73], v[158:159] op_sel_hi:[1,0]
	v_perm_b32 v230, v159, v155, v226
	v_perm_b32 v155, v156, v230, v228
	v_pk_mul_f32 v[156:157], v[74:75], v[158:159] op_sel_hi:[1,0]
	v_add_f32_e32 v159, 0x4b400000, v160
	v_add_f32_e32 v160, 0x4b400000, v161
	v_add_f32_e32 v156, 0x4b400000, v156
	v_add_f32_e32 v157, 0x4b400000, v157
	v_perm_b32 v157, v157, v159, s9
	v_pk_mul_f32 v[162:163], v[68:69], v[158:159] op_sel_hi:[1,0]
	v_perm_b32 v230, v160, v157, v226
	v_perm_b32 v156, v156, v230, v228
	v_pk_mul_f32 v[160:161], v[70:71], v[158:159] op_sel_hi:[1,0]
	v_add_f32_e32 v159, 0x4b400000, v163
	v_add_f32_e32 v157, 0x4b400000, v162
	v_add_f32_e32 v160, 0x4b400000, v160
	v_add_f32_e32 v161, 0x4b400000, v161
	s_nop 0
	v_perm_b32 v157, v161, v157, s9
	v_perm_b32 v230, v159, v157, v226
	v_perm_b32 v157, v160, v230, v228
	v_lshl_add_u64 v[160:161], v[126:127], 0, v[200:201]
	global_store_dwordx4 v[160:161], v[154:157], off
	v_pk_mul_f32 v[160:161], v[92:93], v[158:159] op_sel_hi:[1,0]
	s_nop 0
	v_pk_mul_f32 v[156:157], v[80:81], v[158:159] op_sel_hi:[1,0]
	v_pk_mul_f32 v[154:155], v[82:83], v[158:159] op_sel_hi:[1,0]
	v_add_f32_e32 v157, 0x4b400000, v157
	v_add_f32_e32 v156, 0x4b400000, v156
	s_nop 0
	v_add_f32_e32 v154, 0x4b400000, v154
	v_add_f32_e32 v155, 0x4b400000, v155
	v_perm_b32 v155, v155, v156, s9
	v_perm_b32 v230, v157, v155, v226
	v_perm_b32 v154, v154, v230, v228
	v_pk_mul_f32 v[156:157], v[94:95], v[158:159] op_sel_hi:[1,0]
	v_add_f32_e32 v159, 0x4b400000, v161
	v_add_f32_e32 v155, 0x4b400000, v160
	v_add_f32_e32 v156, 0x4b400000, v156
	v_add_f32_e32 v157, 0x4b400000, v157
	v_perm_b32 v155, v157, v155, s9
	v_pk_mul_f32 v[160:161], v[88:89], v[158:159] op_sel_hi:[1,0]
	v_perm_b32 v230, v159, v155, v226
	v_perm_b32 v155, v156, v230, v228
	v_pk_mul_f32 v[156:157], v[90:91], v[158:159] op_sel_hi:[1,0]
	v_add_f32_e32 v159, 0x4b400000, v160
	v_add_f32_e32 v160, 0x4b400000, v161
	v_add_f32_e32 v156, 0x4b400000, v156
	v_add_f32_e32 v157, 0x4b400000, v157
	s_nop 0
	s_nop 0
	v_perm_b32 v157, v157, v159, s9
	v_perm_b32 v230, v160, v157, v226
	v_perm_b32 v156, v156, v230, v228
	v_pk_mul_f32 v[160:161], v[86:87], v[158:159] op_sel_hi:[1,0]
	v_pk_mul_f32 v[158:159], v[84:85], v[158:159] op_sel_hi:[1,0]
	s_nop 0
	v_add_f32_e32 v157, 0x4b400000, v158
	v_add_f32_e32 v158, 0x4b400000, v159
	s_nop 0
	v_add_f32_e32 v159, 0x4b400000, v160
	v_add_f32_e32 v160, 0x4b400000, v161
	s_nop 0
	s_nop 0
	s_nop 0
	v_perm_b32 v157, v160, v157, s9
	v_perm_b32 v230, v158, v157, v226
	v_perm_b32 v157, v159, v230, v228
	v_lshl_add_u64 v[158:159], v[124:125], 0, v[200:201]
	global_store_dwordx4 v[158:159], v[154:157], off
	s_and_saveexec_b64 s[80:81], s[20:21]
	s_cbranch_execz .LBB0_1846
	v_mul_f32_e32 v153, 0x3c010204, v153
	v_mov_b32_e32 v154, 0x890000
	global_store_dword v154, v153, s[52:53]
	s_branch .LBB0_1846
